# speedup vs baseline: 1.0133x; 1.0133x over previous
.LBB2_22:
	ds_read_b128 v[170:173], v174
	ds_read_b128 v[180:183], v174 offset:2048
	ds_read_b128 v[202:205], v178
	ds_read_b128 v[206:209], v178 offset:2048
	s_mov_b32 s89, s65
	s_mov_b32 s65, s6
	ds_read_b128 v[162:165], v194
	ds_read_b128 v[150:153], v194 offset:2048
	ds_read_b128 v[166:169], v195
	ds_read_b128 v[154:157], v195 offset:2048
	ds_read_b128 v[146:149], v194 offset:4096
	ds_read_b128 v[138:141], v194 offset:6144
	ds_read_b128 v[158:161], v195 offset:4096
	ds_read_b128 v[142:145], v195 offset:6144
	s_waitcnt vmcnt(14)
	s_mul_i32 s94, s83, s35
	v_cvt_pk_f16_f32 v22, v22, v23
	v_cvt_pk_f16_f32 v23, v24, v25
	v_cvt_pk_f16_f32 v18, v18, v19
	v_cvt_pk_f16_f32 v19, v20, v21
	v_cvt_pk_f16_f32 v14, v14, v15
	v_cvt_pk_f16_f32 v15, v16, v17
	v_cvt_pk_f16_f32 v10, v10, v11
	v_cvt_pk_f16_f32 v11, v12, v13
	ds_write2st64_b64 v201, v[22:23], v[18:19] offset0:32 offset1:40
	ds_write2st64_b64 v201, v[14:15], v[10:11] offset0:48 offset1:56
	s_waitcnt vmcnt(12)
	s_lshl_b32 s6, s90, 6
	s_add_i32 s7, s94, s6
	s_lshl_b32 s7, s7, 2
	v_add_u32_e32 v210, s89, v193
	s_add_i32 s8, s7, s81
	s_mul_i32 s95, s84, s35
	ds_write_b128 v210, v[6:9] offset:32768
	ds_write_b128 v210, v[2:5] offset:40960
	s_add_i32 s9, s8, s81
	s_add_i32 s93, s95, s6
	s_add_i32 s10, s9, s81
	s_nop 4
	buffer_load_dwordx4 v[22:25], v192, s[56:59], s7 offen nt
	buffer_load_dwordx4 v[18:21], v192, s[56:59], s8 offen nt
	buffer_load_dwordx4 v[14:17], v192, s[56:59], s9 offen nt
	buffer_load_dwordx4 v[10:13], v192, s[56:59], s10 offen nt
	s_barrier
	s_waitcnt lgkmcnt(0)
	s_setprio 1
	s_waitcnt lgkmcnt(11)
	v_mfma_f32_16x16x32_f16 v[134:137], v[170:173], v[162:165], v[134:137]
	v_mfma_f32_16x16x32_f16 v[130:133], v[180:183], v[162:165], v[130:133]
	s_waitcnt lgkmcnt(10)
	v_mfma_f32_16x16x32_f16 v[126:129], v[170:173], v[150:153], v[126:129]
	v_mfma_f32_16x16x32_f16 v[122:125], v[180:183], v[150:153], v[122:125]
	s_waitcnt lgkmcnt(7)
	v_mfma_f32_16x16x32_f16 v[118:121], v[170:173], v[146:149], v[118:121]
	v_mfma_f32_16x16x32_f16 v[114:117], v[180:183], v[146:149], v[114:117]
	s_waitcnt lgkmcnt(6)
	v_mfma_f32_16x16x32_f16 v[110:113], v[170:173], v[138:141], v[110:113]
	v_mfma_f32_16x16x32_f16 v[106:109], v[180:183], v[138:141], v[106:109]
	v_mfma_f32_16x16x32_f16 v[134:137], v[202:205], v[166:169], v[134:137]
	v_mfma_f32_16x16x32_f16 v[130:133], v[206:209], v[166:169], v[130:133]
	v_mfma_f32_16x16x32_f16 v[126:129], v[202:205], v[154:157], v[126:129]
	v_mfma_f32_16x16x32_f16 v[122:125], v[206:209], v[154:157], v[122:125]
	s_waitcnt lgkmcnt(5)
	v_mfma_f32_16x16x32_f16 v[118:121], v[202:205], v[158:161], v[118:121]
	v_mfma_f32_16x16x32_f16 v[114:117], v[206:209], v[158:161], v[114:117]
	s_waitcnt lgkmcnt(4)
	v_mfma_f32_16x16x32_f16 v[110:113], v[202:205], v[142:145], v[110:113]
	v_mfma_f32_16x16x32_f16 v[106:109], v[206:209], v[142:145], v[106:109]
	s_setprio 0
	s_barrier
	ds_read_b128 v[170:173], v174 offset:16384
	ds_read_b128 v[174:177], v174 offset:18432
	ds_read_b128 v[182:185], v178 offset:16384
	ds_read_b128 v[178:181], v178 offset:18432
	s_waitcnt vmcnt(14)
	s_cmp_lt_u32 s92, 32
	ds_write_b128 v210, v[30:33] offset:49152
	ds_write_b128 v210, v[26:29] offset:57344
	s_waitcnt vmcnt(13)
	s_cbranch_scc0 .LBB2_28
	s_add_i32 s38, s64, s92
	s_lshl_b64 s[60:61], s[38:39], 3
	s_add_u32 s60, s60, s85
	v_cmp_ne_u32_e64 s[6:7], 0, v34
	v_cmp_ne_u32_e64 s[8:9], 0, v35
	v_cmp_ne_u32_e64 s[10:11], 0, v36
	v_cmp_ne_u32_e64 s[12:13], 0, v37
	s_addc_u32 s61, s61, 0
	s_nop 1
	s_and_b64 s[98:99], s[6:7], s[8:9]
	s_and_b64 s[100:101], s[10:11], s[12:13]
	s_and_b64 s[98:99], s[98:99], s[100:101]
	s_cmp_eq_u64 s[98:99], -1
	s_cbranch_scc0 .Lqkv_mslow_0
	s_lshl_b64 s[96:97], s[60:61], 5
	v_lshl_add_u64 v[26:27], v[0:1], 0, s[96:97]
	v_mov_b32_e32 v28, -1
	v_mov_b32_e32 v29, -1
	s_add_u32 s6, s42, s60
	s_addc_u32 s7, s43, s61
	s_mov_b64 exec, 15
	global_store_dwordx2 v[26:27], v[28:29], off
	s_mov_b64 exec, 1
	global_store_byte v187, v187, s[6:7]
	s_mov_b64 exec, -1
	s_branch .LBB2_28

.LBB2_28:
	s_lshl_b32 s6, s93, 1
	s_add_i32 s7, s6, s81
	buffer_load_dwordx4 v[6:9], v191, s[48:51], s6 offen
	buffer_load_dwordx4 v[2:5], v191, s[48:51], s7 offen
	s_add_i32 s93, s93, s81
	s_lshl_b32 s6, s93, 1
	s_add_i32 s91, s92, 2
	s_add_i32 s7, s6, s81
	s_add_i32 s8, s47, 0xffffe000
	s_cmp_lt_u32 s91, 32
	buffer_load_dwordx4 v[30:33], v191, s[48:51], s6 offen
	buffer_load_dwordx4 v[26:29], v191, s[48:51], s7 offen
	s_cselect_b64 s[6:7], -1, 0
	v_cndmask_b32_e64 v202, v200, v190, s[6:7]
	s_and_b64 s[6:7], s[6:7], exec
	s_cselect_b32 s6, s8, 0
	buffer_load_dwordx4 v[34:37], v202, s[52:55], s6 offen nt
	s_add_i32 s90, s90, 1
	s_cmp_lg_u32 s90, s82
	s_cbranch_scc1 .LBB2_32
	s_add_i32 s93, s86, 1
	s_cmp_gt_i32 s86, 1
	s_cbranch_scc1 .LBB2_31
	s_mul_i32 s6, s93, s33
	s_add_i32 s6, s6, s73
	s_abs_i32 s8, s6
	s_mul_hi_u32 s9, s8, s75
	s_mul_i32 s10, s9, s72
	s_ashr_i32 s7, s6, 31
	s_sub_i32 s8, s8, s10
	s_xor_b32 s7, s7, s74
	s_add_i32 s10, s9, 1
	s_sub_i32 s11, s8, s72
	s_cmp_ge_u32 s8, s72
	s_cselect_b32 s9, s10, s9
	s_cselect_b32 s8, s11, s8
	s_add_i32 s10, s9, 1
	s_cmp_ge_u32 s8, s72
	s_cselect_b32 s8, s10, s9
	s_xor_b32 s8, s8, s7
	s_sub_i32 s7, s8, s7
	s_mul_i32 s8, s7, s71
	s_sub_i32 s6, s6, s8
	s_abs_i32 s9, s6
	s_mul_hi_u32 s10, s9, s78
	s_mul_i32 s11, s10, s76
	s_ashr_i32 s8, s6, 31
	s_sub_i32 s9, s9, s11
	s_xor_b32 s8, s8, s77
	s_add_i32 s11, s10, 1
	s_sub_i32 s12, s9, s76
	s_cmp_ge_u32 s9, s76
	s_cselect_b32 s10, s11, s10
	s_cselect_b32 s9, s12, s9
	s_add_i32 s11, s10, 1
	s_cmp_ge_u32 s9, s76
	s_cselect_b32 s9, s11, s10
	s_xor_b32 s9, s9, s8
	s_sub_i32 s8, s9, s8
	s_lshl_b32 s83, s8, 7
	s_mul_i32 s8, s8, s70
	s_sub_i32 s6, s6, s8
	s_lshl_b32 s84, s6, 8
	s_cmp_eq_u32 s7, 1
	s_cselect_b32 s6, s19, s21
	s_cselect_b32 s8, s18, s20
	s_cselect_b32 s9, s25, s27
	s_cselect_b32 s10, s24, s26
	s_cmp_eq_u32 s7, 0
	s_cselect_b32 s6, s17, s6
	s_cselect_b32 s7, s23, s9
	s_cselect_b32 s56, s16, s8
	s_cselect_b32 s48, s22, s10
	s_and_b32 s57, s6, 0xffff
	s_and_b32 s49, s7, 0xffff
	s_mov_b32 s51, s15
	s_mul_i32 s94, s83, s35
	s_mul_i32 s95, s84, s35
	s_mov_b64 s[58:59], s[14:15]

.LBB2_33:
	s_barrier
	s_waitcnt lgkmcnt(0)
	s_setprio 1
	s_waitcnt lgkmcnt(5)
	v_mfma_f32_16x16x32_f16 v[102:105], v[170:173], v[162:165], v[102:105]
	s_waitcnt lgkmcnt(4)
	v_mfma_f32_16x16x32_f16 v[98:101], v[174:177], v[162:165], v[98:101]
	v_mfma_f32_16x16x32_f16 v[94:97], v[170:173], v[150:153], v[94:97]
	v_mfma_f32_16x16x32_f16 v[90:93], v[174:177], v[150:153], v[90:93]
	v_mfma_f32_16x16x32_f16 v[86:89], v[170:173], v[146:149], v[86:89]
	v_mfma_f32_16x16x32_f16 v[82:85], v[174:177], v[146:149], v[82:85]
	v_mfma_f32_16x16x32_f16 v[78:81], v[170:173], v[138:141], v[78:81]
	v_mfma_f32_16x16x32_f16 v[74:77], v[174:177], v[138:141], v[74:77]
	s_waitcnt lgkmcnt(3)
	v_mfma_f32_16x16x32_f16 v[102:105], v[182:185], v[166:169], v[102:105]
	s_waitcnt lgkmcnt(2)
	v_mfma_f32_16x16x32_f16 v[98:101], v[178:181], v[166:169], v[98:101]
	v_mfma_f32_16x16x32_f16 v[94:97], v[182:185], v[154:157], v[94:97]
	v_mfma_f32_16x16x32_f16 v[90:93], v[178:181], v[154:157], v[90:93]
	v_mfma_f32_16x16x32_f16 v[86:89], v[182:185], v[158:161], v[86:89]
	v_mfma_f32_16x16x32_f16 v[82:85], v[178:181], v[158:161], v[82:85]
	v_mfma_f32_16x16x32_f16 v[78:81], v[182:185], v[142:145], v[78:81]
	v_mfma_f32_16x16x32_f16 v[74:77], v[178:181], v[142:145], v[74:77]
	s_setprio 0
	s_barrier
	v_add_u32_e32 v202, s89, v196
	v_add_u32_e32 v203, s89, v186
	ds_read_b128 v[170:173], v202 offset:32768
	ds_read_b128 v[174:177], v202 offset:34816
	ds_read_b128 v[178:181], v203 offset:32768
	ds_read_b128 v[182:185], v203 offset:34816
	ds_read_b128 v[162:165], v194 offset:16384
	ds_read_b128 v[150:153], v194 offset:18432
	ds_read_b128 v[166:169], v195 offset:16384
	ds_read_b128 v[154:157], v195 offset:18432
	ds_read_b128 v[146:149], v194 offset:20480
	ds_read_b128 v[138:141], v194 offset:22528
	ds_read_b128 v[158:161], v195 offset:20480
	ds_read_b128 v[142:145], v195 offset:22528
	s_waitcnt vmcnt(14)
	s_lshl_b32 s86, s90, 6
	v_cvt_pk_f16_f32 v58, v58, v59
	v_cvt_pk_f16_f32 v59, v60, v61
	v_cvt_pk_f16_f32 v54, v54, v55
	v_cvt_pk_f16_f32 v55, v56, v57
	v_cvt_pk_f16_f32 v50, v50, v51
	v_cvt_pk_f16_f32 v51, v52, v53
	v_cvt_pk_f16_f32 v46, v46, v47
	v_cvt_pk_f16_f32 v47, v48, v49
	ds_write2st64_b64 v201, v[58:59], v[54:55] offset1:8
	ds_write2st64_b64 v201, v[50:51], v[46:47] offset0:16 offset1:24
	s_waitcnt vmcnt(12)
	s_add_i32 s6, s94, s86
	s_lshl_b32 s6, s6, 2
	v_add_u32_e32 v204, s87, v193
	s_add_i32 s7, s6, s81
	ds_write_b128 v204, v[42:45] offset:32768
	ds_write_b128 v204, v[38:41] offset:40960
	s_add_i32 s8, s7, s81
	s_add_i32 s9, s8, s81
	s_nop 4
	buffer_load_dwordx4 v[58:61], v192, s[56:59], s6 offen nt
	buffer_load_dwordx4 v[54:57], v192, s[56:59], s7 offen nt
	buffer_load_dwordx4 v[50:53], v192, s[56:59], s8 offen nt
	buffer_load_dwordx4 v[46:49], v192, s[56:59], s9 offen nt
	s_barrier
	s_waitcnt lgkmcnt(0)
	s_setprio 1
	s_waitcnt lgkmcnt(11)
	v_mfma_f32_16x16x32_f16 v[134:137], v[170:173], v[162:165], v[134:137]
	v_mfma_f32_16x16x32_f16 v[130:133], v[174:177], v[162:165], v[130:133]
	s_waitcnt lgkmcnt(10)
	v_mfma_f32_16x16x32_f16 v[126:129], v[170:173], v[150:153], v[126:129]
	v_mfma_f32_16x16x32_f16 v[122:125], v[174:177], v[150:153], v[122:125]
	s_waitcnt lgkmcnt(7)
	v_mfma_f32_16x16x32_f16 v[118:121], v[170:173], v[146:149], v[118:121]
	v_mfma_f32_16x16x32_f16 v[114:117], v[174:177], v[146:149], v[114:117]
	s_waitcnt lgkmcnt(6)
	v_mfma_f32_16x16x32_f16 v[110:113], v[170:173], v[138:141], v[110:113]
	v_mfma_f32_16x16x32_f16 v[106:109], v[174:177], v[138:141], v[106:109]
	v_mfma_f32_16x16x32_f16 v[134:137], v[178:181], v[166:169], v[134:137]
	v_mfma_f32_16x16x32_f16 v[130:133], v[182:185], v[166:169], v[130:133]
	v_mfma_f32_16x16x32_f16 v[126:129], v[178:181], v[154:157], v[126:129]
	v_mfma_f32_16x16x32_f16 v[122:125], v[182:185], v[154:157], v[122:125]
	s_waitcnt lgkmcnt(5)
	v_mfma_f32_16x16x32_f16 v[118:121], v[178:181], v[158:161], v[118:121]
	v_mfma_f32_16x16x32_f16 v[114:117], v[182:185], v[158:161], v[114:117]
	s_waitcnt lgkmcnt(4)
	v_mfma_f32_16x16x32_f16 v[110:113], v[178:181], v[142:145], v[110:113]
	v_mfma_f32_16x16x32_f16 v[106:109], v[182:185], v[142:145], v[106:109]
	s_setprio 0
	s_barrier
	ds_read_b128 v[170:173], v202 offset:49152
	ds_read_b128 v[174:177], v202 offset:51200
	ds_read_b128 v[182:185], v203 offset:49152
	ds_read_b128 v[178:181], v203 offset:51200
	s_waitcnt vmcnt(14)
	s_cmp_gt_u32 s92, 30
	ds_write_b128 v204, v[66:69] offset:49152
	ds_write_b128 v204, v[62:65] offset:57344
	s_waitcnt vmcnt(13)
	s_cbranch_scc1 .LBB2_39
	s_add_i32 s38, s64, s92
	s_add_i32 s38, s38, 1
	s_lshl_b64 s[60:61], s[38:39], 3
	s_add_u32 s60, s60, s85
	v_cmp_ne_u32_e64 s[6:7], 0, v70
	v_cmp_ne_u32_e64 s[8:9], 0, v71
	v_cmp_ne_u32_e64 s[10:11], 0, v72
	v_cmp_ne_u32_e64 s[12:13], 0, v73
	s_addc_u32 s61, s61, 0
	s_nop 1
	s_and_b64 s[98:99], s[6:7], s[8:9]
	s_and_b64 s[100:101], s[10:11], s[12:13]
	s_and_b64 s[98:99], s[98:99], s[100:101]
	s_cmp_eq_u64 s[98:99], -1
	s_cbranch_scc0 .Lqkv_mslow_1
	s_lshl_b64 s[94:95], s[60:61], 5
	v_lshl_add_u64 v[62:63], v[0:1], 0, s[94:95]
	v_mov_b32_e32 v64, -1
	v_mov_b32_e32 v65, -1
	s_add_u32 s6, s42, s60
	s_addc_u32 s7, s43, s61
	s_mov_b64 exec, 15
	global_store_dwordx2 v[62:63], v[64:65], off
	s_mov_b64 exec, 1
	global_store_byte v187, v187, s[6:7]
	s_mov_b64 exec, -1
	s_branch .LBB2_39

.LBB2_39:
	s_add_i32 s6, s84, 0x80
	s_mul_i32 s6, s6, s35
	s_add_i32 s6, s6, s86
	s_lshl_b32 s6, s6, 1
	s_sub_i32 s9, s6, s81
	s_sub_i32 s8, s9, s81
	s_add_i32 s7, s6, s81
	buffer_load_dwordx4 v[42:45], v191, s[48:51], s8 offen
	buffer_load_dwordx4 v[38:41], v191, s[48:51], s9 offen
	s_cmp_lt_u32 s91, 31
	buffer_load_dwordx4 v[66:69], v191, s[48:51], s6 offen
	buffer_load_dwordx4 v[62:65], v191, s[48:51], s7 offen
	s_cselect_b64 s[6:7], -1, 0
	v_cndmask_b32_e64 v202, v200, v190, s[6:7]
	s_and_b64 s[6:7], s[6:7], exec
	s_cselect_b32 s6, s47, 0
	buffer_load_dwordx4 v[70:73], v202, s[52:55], s6 offen nt
	s_add_i32 s90, s90, 1
	s_cmp_lg_u32 s90, s82
	s_cbranch_scc1 .LBB2_43
	s_add_i32 s86, s93, 1
	s_cmp_gt_i32 s93, 1
	s_cbranch_scc1 .LBB2_42
	s_mul_i32 s6, s86, s33
	s_add_i32 s6, s6, s73
	s_abs_i32 s8, s6
	s_mul_hi_u32 s9, s8, s75
	s_mul_i32 s10, s9, s72
	s_ashr_i32 s7, s6, 31
	s_sub_i32 s8, s8, s10
	s_xor_b32 s7, s7, s74
	s_add_i32 s10, s9, 1
	s_sub_i32 s11, s8, s72
	s_cmp_ge_u32 s8, s72
	s_cselect_b32 s9, s10, s9
	s_cselect_b32 s8, s11, s8
	s_add_i32 s10, s9, 1
	s_cmp_ge_u32 s8, s72
	s_cselect_b32 s8, s10, s9
	s_xor_b32 s8, s8, s7
	s_sub_i32 s7, s8, s7
	s_mul_i32 s8, s7, s71
	s_sub_i32 s6, s6, s8
	s_abs_i32 s9, s6
	s_mul_hi_u32 s10, s9, s78
	s_mul_i32 s11, s10, s76
	s_ashr_i32 s8, s6, 31
	s_sub_i32 s9, s9, s11
	s_xor_b32 s8, s8, s77
	s_add_i32 s11, s10, 1
	s_sub_i32 s12, s9, s76
	s_cmp_ge_u32 s9, s76
	s_cselect_b32 s10, s11, s10
	s_cselect_b32 s9, s12, s9
	s_add_i32 s11, s10, 1
	s_cmp_ge_u32 s9, s76
	s_cselect_b32 s9, s11, s10
	s_xor_b32 s9, s9, s8
	s_sub_i32 s8, s9, s8
	s_lshl_b32 s83, s8, 7
	s_mul_i32 s8, s8, s70
	s_sub_i32 s6, s6, s8
	s_lshl_b32 s84, s6, 8
	s_cmp_eq_u32 s7, 1
	s_cselect_b32 s6, s19, s21
	s_cselect_b32 s8, s18, s20
	s_cselect_b32 s9, s25, s27
	s_cselect_b32 s10, s24, s26
	s_cmp_eq_u32 s7, 0
	s_cselect_b32 s6, s17, s6
	s_cselect_b32 s7, s23, s9
	s_cselect_b32 s56, s16, s8
	s_cselect_b32 s48, s22, s10
	s_and_b32 s57, s6, 0xffff
	s_and_b32 s49, s7, 0xffff
	s_mov_b32 s51, s15
	s_mov_b64 s[58:59], s[14:15]

.LBB2_48:
	s_endpgm
	s_nop 0
	s_nop 0
	s_nop 0
	s_nop 0
	s_nop 0
	s_nop 0
	s_nop 0
	s_nop 0
	s_nop 0
	s_nop 0
	s_nop 0
	s_nop 0
	s_nop 0
	s_endpgm
